# speedup vs baseline: 1.0120x; 1.0120x over previous
.Lmain_noprio:
	s_waitcnt lgkmcnt(0)
	s_and_b32 s13, s13, 0xffff
	v_lshlrev_b32_e32 v105, 9, v112
	v_lshlrev_b32_e32 v2, 6, v112
	v_lshlrev_b32_e32 v3, 4, v1
	s_cmp_lt_u32 s44, s42
	s_mov_b32 s7, 0x20000
	v_bitop3_b32 v113, v2, v105, v3 bitop3:0xde
	s_mov_b32 s6, 0x1e848000
	s_cselect_b64 s[8:9], -1, 0
	v_lshlrev_b32_e32 v102, 2, v1
	v_lshlrev_b32_e32 v14, 4, v104
	v_mov_b32_e32 v15, 0
	v_lshl_add_u64 v[6:7], s[16:17], 0, v[14:15]
	v_add_co_u32_e32 v16, vcc, 0x3000, v6
	v_min_u32_e32 v6, 0x1ff, v104
	s_nop 0
	v_addc_co_u32_e32 v17, vcc, 0, v7, vcc
	v_lshlrev_b32_e32 v7, 2, v6
	global_load_dword v15, v7, s[10:11]
	global_load_dwordx4 v[2:5], v14, s[16:17]
	v_lshlrev_b32_e32 v18, 4, v6
	v_or_b32_e32 v19, 0x6000, v18
	global_load_dwordx4 v[6:9], v[16:17], off
	global_load_dwordx4 v[10:13], v19, s[16:17]
	v_min_u32_e32 v16, 0x17f, v104
	v_lshlrev_b32_e32 v16, 2, v16
	global_load_dword v17, v16, s[18:19]
	s_cmp_ge_u32 s44, s42
	s_cbranch_scc1 .Lmain_nodma
	s_lshl_b32 s2, s44, 13
	s_mov_b32 s4, s12
	s_mov_b32 s5, s13
	s_bitcmp1_b32 s3, 0
	s_cbranch_scc1 .Lmain_dma_rev
	s_add_i32 m0, s33, 0x8000
	s_or_b32 s3, s2, 0x0
	buffer_load_dwordx4 v113, s[4:7], s3 offen nt lds
	s_add_i32 m0, s33, 0x8400
	s_or_b32 s3, s2, 0x800
	buffer_load_dwordx4 v113, s[4:7], s3 offen nt lds
	s_add_i32 m0, s33, 0x8800
	s_or_b32 s3, s2, 0x1000
	buffer_load_dwordx4 v113, s[4:7], s3 offen nt lds
	s_add_i32 m0, s33, 0x8c00
	s_or_b32 s3, s2, 0x1800
	buffer_load_dwordx4 v113, s[4:7], s3 offen nt lds
	s_add_i32 m0, s33, 0x9000
	s_or_b32 s3, s2, 0x100
	buffer_load_dwordx4 v113, s[4:7], s3 offen nt lds
	s_add_i32 m0, s33, 0x9400
	s_or_b32 s3, s2, 0x900
	buffer_load_dwordx4 v113, s[4:7], s3 offen nt lds
	s_add_i32 m0, s33, 0x9800
	s_or_b32 s3, s2, 0x1100
	buffer_load_dwordx4 v113, s[4:7], s3 offen nt lds
	s_add_i32 m0, s33, 0x9c00
	s_or_b32 s3, s2, 0x1900
	buffer_load_dwordx4 v113, s[4:7], s3 offen nt lds
	s_branch .Lmain_dma_ids
.Lmain_dma_rev:
	s_add_i32 m0, s33, 0x9c00
	s_or_b32 s3, s2, 0x1900
	buffer_load_dwordx4 v113, s[4:7], s3 offen nt lds
	s_add_i32 m0, s33, 0x9800
	s_or_b32 s3, s2, 0x1100
	buffer_load_dwordx4 v113, s[4:7], s3 offen nt lds
	s_add_i32 m0, s33, 0x9400
	s_or_b32 s3, s2, 0x900
	buffer_load_dwordx4 v113, s[4:7], s3 offen nt lds
	s_add_i32 m0, s33, 0x9000
	s_or_b32 s3, s2, 0x100
	buffer_load_dwordx4 v113, s[4:7], s3 offen nt lds
	s_add_i32 m0, s33, 0x8c00
	s_or_b32 s3, s2, 0x1800
	buffer_load_dwordx4 v113, s[4:7], s3 offen nt lds
	s_add_i32 m0, s33, 0x8800
	s_or_b32 s3, s2, 0x1000
	buffer_load_dwordx4 v113, s[4:7], s3 offen nt lds
	s_add_i32 m0, s33, 0x8400
	s_or_b32 s3, s2, 0x800
	buffer_load_dwordx4 v113, s[4:7], s3 offen nt lds
	s_add_i32 m0, s33, 0x8000
	s_or_b32 s3, s2, 0x0
	buffer_load_dwordx4 v113, s[4:7], s3 offen nt lds
.Lmain_dma_ids:
	s_lshl_b32 s2, s44, 6
	s_add_u32 s2, s14, s2
	s_addc_u32 s3, s15, 0
	s_mov_b32 m0, s43
	s_nop 0
	global_load_lds_dword v102, s[2:3]
